# P2 stage I: LDS reads of round k+1 issued ahead of round k's MFMAs (second operand set in free VGPRs, counted lgkmcnt); stacked on combined version
# speedup vs baseline: 1.0000x; 1.0000x over previous
.LBB0_372:
	v_lshlrev_b32_e32 v1, 10, v2
	v_lshlrev_b32_e32 v2, 1, v16
	v_add3_u32 v1, s26, v1, v2
	s_nop 7
	v_bfe_u32 v2, v50, 16, 1
	v_add3_u32 v2, v50, v2, s19
	ds_write_b16_d16_hi v1, v2
	v_bfe_u32 v2, v51, 16, 1
	v_add3_u32 v2, v51, v2, s19
	ds_write_b16_d16_hi v1, v2 offset:256
	v_bfe_u32 v2, v52, 16, 1
	v_add3_u32 v2, v52, v2, s19
	ds_write_b16_d16_hi v1, v2 offset:512
	v_bfe_u32 v2, v53, 16, 1
	v_add3_u32 v2, v53, v2, s19
	ds_write_b16_d16_hi v1, v2 offset:768
	v_bfe_u32 v2, v54, 16, 1
	v_add3_u32 v2, v54, v2, s19
	ds_write_b16_d16_hi v1, v2 offset:2048
	v_bfe_u32 v2, v55, 16, 1
	v_add3_u32 v2, v55, v2, s19
	ds_write_b16_d16_hi v1, v2 offset:2304
	v_bfe_u32 v2, v56, 16, 1
	v_add3_u32 v2, v56, v2, s19
	ds_write_b16_d16_hi v1, v2 offset:2560
	v_bfe_u32 v2, v57, 16, 1
	v_add3_u32 v2, v57, v2, s19
	ds_write_b16_d16_hi v1, v2 offset:2816
	v_bfe_u32 v2, v58, 16, 1
	v_add3_u32 v2, v58, v2, s19
	ds_write_b16_d16_hi v1, v2 offset:4096
	v_bfe_u32 v2, v59, 16, 1
	v_add3_u32 v2, v59, v2, s19
	ds_write_b16_d16_hi v1, v2 offset:4352
	v_bfe_u32 v2, v60, 16, 1
	v_add3_u32 v2, v60, v2, s19
	ds_write_b16_d16_hi v1, v2 offset:4608
	v_bfe_u32 v2, v61, 16, 1
	v_add3_u32 v2, v61, v2, s19
	ds_write_b16_d16_hi v1, v2 offset:4864
	v_bfe_u32 v2, v62, 16, 1
	v_add3_u32 v2, v62, v2, s19
	ds_write_b16_d16_hi v1, v2 offset:6144
	v_bfe_u32 v2, v63, 16, 1
	v_add3_u32 v2, v63, v2, s19
	ds_write_b16_d16_hi v1, v2 offset:6400
	v_bfe_u32 v2, v64, 16, 1
	v_add3_u32 v2, v64, v2, s19
	ds_write_b16_d16_hi v1, v2 offset:6656
	v_bfe_u32 v2, v65, 16, 1
	v_add3_u32 v2, v65, v2, s19
	ds_write_b16_d16_hi v1, v2 offset:6912
	v_mov_b32_e32 v1, s8
	ds_read_b32 v2, v1
	v_lshrrev_b32_e32 v4, 3, v186
	v_and_b32_e32 v4, 2, v4
	v_bfe_u32 v5, v186, 1, 1
	v_or3_b32 v6, v5, v4, s3
	s_waitcnt lgkmcnt(0)
	v_pk_mul_f32 v[32:33], v[32:33], v[2:3] op_sel_hi:[1,0]
	v_pk_mul_f32 v[30:31], v[30:31], v[2:3] op_sel_hi:[1,0]
	v_pk_mul_f32 v[28:29], v[28:29], v[2:3] op_sel_hi:[1,0]
	v_pk_mul_f32 v[26:27], v[26:27], v[2:3] op_sel_hi:[1,0]
	v_pk_mul_f32 v[24:25], v[24:25], v[2:3] op_sel_hi:[1,0]
	v_pk_mul_f32 v[22:23], v[22:23], v[2:3] op_sel_hi:[1,0]
	v_pk_mul_f32 v[20:21], v[20:21], v[2:3] op_sel_hi:[1,0]
	v_pk_mul_f32 v[18:19], v[18:19], v[2:3] op_sel_hi:[1,0]
	v_pk_mul_f32 v[48:49], v[48:49], v[2:3] op_sel_hi:[1,0]
	v_pk_mul_f32 v[46:47], v[46:47], v[2:3] op_sel_hi:[1,0]
	v_pk_mul_f32 v[44:45], v[44:45], v[2:3] op_sel_hi:[1,0]
	v_pk_mul_f32 v[42:43], v[42:43], v[2:3] op_sel_hi:[1,0]
	v_pk_mul_f32 v[40:41], v[40:41], v[2:3] op_sel_hi:[1,0]
	v_pk_mul_f32 v[38:39], v[38:39], v[2:3] op_sel_hi:[1,0]
	v_pk_mul_f32 v[36:37], v[36:37], v[2:3] op_sel_hi:[1,0]
	v_pk_mul_f32 v[34:35], v[34:35], v[2:3] op_sel_hi:[1,0]
	v_bfe_u32 v2, v186, 2, 2
	v_lshrrev_b32_e32 v4, 4, v186
	v_bfe_u32 v16, v186, 5, 1
	v_lshlrev_b32_e32 v7, 2, v2
	v_and_b32_e32 v4, 2, v4
	v_lshlrev_b32_e32 v17, 3, v16
	v_bitop3_b32 v4, v7, v6, v4 bitop3:0x36
	v_lshlrev_b32_e32 v5, 3, v186
	v_lshl_or_b32 v7, v16, 1, v7
	v_and_or_b32 v9, v5, 8, 0
	v_or_b32_e32 v5, v17, v2
	v_bitop3_b32 v6, v7, v6, 1 bitop3:0x36
	v_and_b32_e32 v1, 31, v186
	v_lshrrev_b32_e32 v8, 5, v186
	v_lshlrev_b32_e32 v4, 4, v4
	v_and_b32_e32 v50, 7, v186
	v_lshlrev_b32_e32 v10, 8, v5
	v_lshlrev_b32_e32 v6, 4, v6
	v_lshl_add_u32 v51, v1, 7, s72
	v_add3_u32 v52, v4, v9, v10
	ds_read_b64_tr_b16 v[4:5], v52
	v_add3_u32 v53, v6, v9, v10
	v_bitop3_b32 v8, v8, v50, 1 bitop3:0x6c
	v_add_u32_e32 v9, 0x400, v53
	ds_read_b64_tr_b16 v[6:7], v9
	v_lshl_add_u32 v12, v8, 4, v51
	ds_read_b128 v[8:11], v12
	ds_read_b128 v[12:15], v12 offset:4096
	v_add_u32_e32 v240, 0x1000, v52
	v_add_u32_e32 v241, 0x1400, v53
	ds_read_b64_tr_b16 v[228:229], v240
	ds_read_b64_tr_b16 v[230:231], v241
	v_bitop3_b32 v242, v16, v50, 2 bitop3:0x36
	v_lshl_add_u32 v242, v242, 4, v51
	ds_read_b128 v[232:235], v242
	ds_read_b128 v[236:239], v242 offset:4096
	s_waitcnt lgkmcnt(5)
	v_mfma_f32_32x32x16_bf16 v[18:33], v[4:7], v[8:11], v[18:33]
	s_waitcnt lgkmcnt(4)
	v_mfma_f32_32x32x16_bf16 v[34:49], v[4:7], v[12:15], v[34:49]
	v_add_u32_e32 v240, 0x2000, v52
	v_add_u32_e32 v241, 0x2400, v53
	ds_read_b64_tr_b16 v[4:5], v240
	ds_read_b64_tr_b16 v[6:7], v241
	v_bitop3_b32 v242, v16, v50, 4 bitop3:0x36
	v_lshl_add_u32 v242, v242, 4, v51
	ds_read_b128 v[8:11], v242
	ds_read_b128 v[12:15], v242 offset:4096
	s_waitcnt lgkmcnt(5)
	v_mfma_f32_32x32x16_bf16 v[18:33], v[228:231], v[232:235], v[18:33]
	s_waitcnt lgkmcnt(4)
	v_mfma_f32_32x32x16_bf16 v[34:49], v[228:231], v[236:239], v[34:49]
	v_add_u32_e32 v240, 0x3000, v52
	v_add_u32_e32 v241, 0x3400, v53
	ds_read_b64_tr_b16 v[228:229], v240
	ds_read_b64_tr_b16 v[230:231], v241
	v_bitop3_b32 v242, v16, v50, 6 bitop3:0x36
	v_lshl_add_u32 v242, v242, 4, v51
	ds_read_b128 v[232:235], v242
	ds_read_b128 v[236:239], v242 offset:4096
	s_waitcnt lgkmcnt(5)
	v_mfma_f32_32x32x16_bf16 v[18:33], v[4:7], v[8:11], v[18:33]
	s_waitcnt lgkmcnt(4)
	v_mfma_f32_32x32x16_bf16 v[34:49], v[4:7], v[12:15], v[34:49]
	s_waitcnt lgkmcnt(1)
	v_mfma_f32_32x32x16_bf16 v[18:33], v[228:231], v[232:235], v[18:33]
	v_lshl_add_u32 v1, v1, 8, 0
	v_add3_u32 v1, v1, v17, s73
	s_waitcnt vmcnt(0)
	v_lshlrev_b32_e32 v64, 16, v148
	v_and_b32_e32 v65, 0xffff0000, v148
	v_lshlrev_b32_e32 v70, 16, v147
	v_and_b32_e32 v71, 0xffff0000, v147
	v_lshlrev_b32_e32 v80, 16, v145
	s_waitcnt lgkmcnt(0)
	v_mfma_f32_32x32x16_bf16 v[34:49], v[228:231], v[236:239], v[34:49]
	v_lshlrev_b32_e32 v4, 2, v186
	v_and_b32_e32 v8, 12, v4
	v_bitop3_b32 v6, v8, s3, v2 bitop3:0x36
	v_bitop3_b32 v10, v8, s56, v2 bitop3:0x36
	v_lshl_add_u32 v9, v6, 4, v1
	v_cvt_pk_bf16_f32 v6, v22, v23
	v_cvt_pk_bf16_f32 v7, v24, v25
	v_lshl_add_u32 v10, v10, 4, v1
	v_bitop3_b32 v11, v8, s57, v2 bitop3:0x36
	ds_write_b64 v10, v[6:7] offset:49152
	v_cvt_pk_bf16_f32 v6, v26, v27
	v_cvt_pk_bf16_f32 v7, v28, v29
	v_lshl_add_u32 v11, v11, 4, v1
	v_bitop3_b32 v2, v8, s62, v2 bitop3:0x36
	ds_write_b64 v11, v[6:7] offset:49152
	v_cvt_pk_bf16_f32 v6, v30, v31
	v_cvt_pk_bf16_f32 v7, v32, v33
	v_lshl_add_u32 v1, v2, 4, v1
	v_cvt_pk_bf16_f32 v4, v18, v19
	v_cvt_pk_bf16_f32 v5, v20, v21
	ds_write_b64 v1, v[6:7] offset:49152
	v_cvt_pk_bf16_f32 v6, v34, v35
	v_cvt_pk_bf16_f32 v7, v36, v37
	ds_write2st64_b64 v9, v[4:5], v[6:7] offset0:96 offset1:112
	v_cvt_pk_bf16_f32 v4, v38, v39
	v_cvt_pk_bf16_f32 v5, v40, v41
	ds_write_b64 v10, v[4:5] offset:57344
	v_cvt_pk_bf16_f32 v4, v42, v43
	v_cvt_pk_bf16_f32 v5, v44, v45
	ds_write_b64 v11, v[4:5] offset:57344
	v_cvt_pk_bf16_f32 v4, v46, v47
	v_cvt_pk_bf16_f32 v5, v48, v49
	ds_write_b64 v1, v[4:5] offset:57344
	s_waitcnt lgkmcnt(0)
	s_barrier
	v_and_b32_e32 v81, 0xffff0000, v145
	v_ashrrev_i32_e32 v16, 3, v186
	v_and_b32_e32 v1, 7, v186
	v_lshlrev_b32_e32 v4, 8, v16
	v_lshlrev_b32_e32 v2, 5, v1
	v_add3_u32 v4, s18, v4, v2
	ds_read_b128 v[54:57], v4
	ds_read_b128 v[74:77], v4 offset:16
	v_lshl_add_u32 v1, v1, 6, 0
	v_add_u32_e32 v1, 0x22000, v1
	ds_read_b128 v[50:53], v1
	ds_read_b128 v[12:15], v1 offset:16
	ds_read_b128 v[8:11], v1 offset:32
	ds_read_b128 v[4:7], v1 offset:48
	v_mul_f32_e32 v1, 0xbfb8aa3b, v64
	v_exp_f32_e32 v1, v1
	s_waitcnt lgkmcnt(4)
	v_and_b32_e32 v61, 0xffff0000, v77
	v_and_b32_e32 v63, 0xffff0000, v76
	v_lshlrev_b32_e32 v60, 16, v77
	v_lshlrev_b32_e32 v62, 16, v76
	v_mov_b32_e32 v68, v61
	v_mov_b32_e32 v69, v63
	v_mov_b32_e32 v66, v60
	v_mov_b32_e32 v67, v62
	v_pk_mul_f32 v[68:69], v[68:69], v[68:69]
	v_add_f32_e32 v1, 1.0, v1
	v_pk_fma_f32 v[68:69], v[66:67], v[66:67], v[68:69]
	v_rcp_f32_e32 v66, v1
	v_mul_f32_e32 v1, 0xbfb8aa3b, v65
	v_exp_f32_e32 v1, v1
	v_lshlrev_b32_e32 v58, 16, v149
	v_and_b32_e32 v59, 0xffff0000, v149
	v_lshlrev_b32_e32 v152, 16, v143
	v_add_f32_e32 v1, 1.0, v1
	v_rcp_f32_e32 v67, v1
	v_mul_f32_e32 v1, 0xbfb8aa3b, v70
	v_exp_f32_e32 v1, v1
	v_and_b32_e32 v153, 0xffff0000, v143
	v_pk_mul_f32 v[64:65], v[66:67], v[64:65]
	v_and_b32_e32 v67, 0xffff0000, v75
	v_add_f32_e32 v1, 1.0, v1
	v_rcp_f32_e32 v72, v1
	v_mul_f32_e32 v1, 0xbfb8aa3b, v71
	v_exp_f32_e32 v1, v1
	v_lshlrev_b32_e32 v66, 16, v75
	v_mov_b32_e32 v78, v67
	v_and_b32_e32 v75, 0xffff0000, v146
	v_add_f32_e32 v1, 1.0, v1
	v_rcp_f32_e32 v73, v1
	v_mov_b32_e32 v76, v66
	s_add_u32 s88, s88, 64
	s_addc_u32 s89, s89, 0
	v_pk_mul_f32 v[70:71], v[72:73], v[70:71]
	v_lshlrev_b32_e32 v72, 16, v74
	v_and_b32_e32 v73, 0xffff0000, v74
	v_lshlrev_b32_e32 v74, 16, v146
	v_mul_f32_e32 v1, 0xbfb8aa3b, v74
	v_exp_f32_e32 v1, v1
	v_mov_b32_e32 v79, v73
	v_mov_b32_e32 v77, v72
	v_pk_mul_f32 v[78:79], v[78:79], v[78:79]
	v_add_f32_e32 v1, 1.0, v1
	v_pk_fma_f32 v[78:79], v[76:77], v[76:77], v[78:79]
	v_rcp_f32_e32 v76, v1
	v_mul_f32_e32 v1, 0xbfb8aa3b, v75
	v_exp_f32_e32 v1, v1
	s_cmpk_eq_i32 s88, 0x800
	v_add_f32_e32 v1, 1.0, v1
	v_rcp_f32_e32 v77, v1
	v_mul_f32_e32 v1, 0xbfb8aa3b, v80
	v_exp_f32_e32 v1, v1
	v_pk_mul_f32 v[74:75], v[76:77], v[74:75]
	v_lshlrev_b32_e32 v76, 16, v57
	v_add_f32_e32 v1, 1.0, v1
	v_rcp_f32_e32 v148, v1
	v_mul_f32_e32 v1, 0xbfb8aa3b, v81
	v_exp_f32_e32 v1, v1
	v_and_b32_e32 v77, 0xffff0000, v57
	v_and_b32_e32 v57, 0xffff0000, v144
	v_pk_mul_f32 v[146:147], v[76:77], v[76:77]
	v_add_f32_e32 v1, 1.0, v1
	v_rcp_f32_e32 v149, v1
	s_nop 0
	v_pk_mul_f32 v[80:81], v[148:149], v[80:81]
	v_lshlrev_b32_e32 v148, 16, v56
	v_and_b32_e32 v149, 0xffff0000, v56
	v_lshlrev_b32_e32 v56, 16, v144
	v_mul_f32_e32 v1, 0xbfb8aa3b, v56
	v_exp_f32_e32 v1, v1
	v_pk_mul_f32 v[144:145], v[148:149], v[148:149]
	v_add_f32_e32 v1, 1.0, v1
	v_rcp_f32_e32 v150, v1
	v_mul_f32_e32 v1, 0xbfb8aa3b, v57
	v_exp_f32_e32 v1, v1
	s_nop 0
	v_add_f32_e32 v1, 1.0, v1
	v_rcp_f32_e32 v151, v1
	v_mul_f32_e32 v1, 0xbfb8aa3b, v152
	v_exp_f32_e32 v1, v1
	v_pk_mul_f32 v[56:57], v[150:151], v[56:57]
	v_lshlrev_b32_e32 v150, 16, v55
	v_add_f32_e32 v1, 1.0, v1
	v_rcp_f32_e32 v156, v1
	v_mul_f32_e32 v1, 0xbfb8aa3b, v153
	v_exp_f32_e32 v1, v1
	v_and_b32_e32 v151, 0xffff0000, v55
	v_and_b32_e32 v55, 0xffff0000, v142
	v_pk_mul_f32 v[154:155], v[150:151], v[150:151]
	v_add_f32_e32 v1, 1.0, v1
	v_rcp_f32_e32 v157, v1
	v_add_f32_e32 v17, v154, v155
	v_pk_mul_f32 v[152:153], v[156:157], v[152:153]
	v_lshlrev_b32_e32 v156, 16, v54
	v_and_b32_e32 v157, 0xffff0000, v54
	v_lshlrev_b32_e32 v54, 16, v142
	v_mul_f32_e32 v1, 0xbfb8aa3b, v54
	v_exp_f32_e32 v1, v1
	v_pk_mul_f32 v[142:143], v[156:157], v[156:157]
	v_add_f32_e32 v1, 1.0, v1
	v_rcp_f32_e32 v158, v1
	v_mul_f32_e32 v1, 0xbfb8aa3b, v55
	v_exp_f32_e32 v1, v1
	v_add_f32_e32 v142, v142, v143
	v_add_f32_e32 v17, v142, v17
	v_add_f32_e32 v142, v144, v145
	v_add_f32_e32 v1, 1.0, v1
	v_rcp_f32_e32 v159, v1
	v_add_f32_e32 v1, v146, v147
	v_add_f32_e32 v17, v142, v17
	v_add_f32_e32 v1, v1, v17
	v_add_f32_e32 v1, v79, v1
	v_add_f32_e32 v1, v78, v1
	v_add_f32_e32 v1, v69, v1
	v_add_f32_e32 v1, v68, v1
	v_pk_mul_f32 v[54:55], v[158:159], v[54:55]
	s_nop 0
	v_add_f32_dpp v1, v1, v1 quad_perm:[1,0,3,2] row_mask:0xf bank_mask:0xf bound_ctrl:1
	s_nop 1
	v_add_f32_dpp v1, v1, v1 quad_perm:[2,3,0,1] row_mask:0xf bank_mask:0xf bound_ctrl:1
	s_nop 1
	v_add_f32_dpp v1, v1, v1 row_half_mirror row_mask:0xf bank_mask:0xf bound_ctrl:1
	v_fmamk_f32 v1, v1, 0x3c000000, v202
	v_cmp_gt_f32_e32 vcc, s64, v1
	v_mul_f32_e32 v17, 0x4f800000, v1
	s_nop 0
	v_cndmask_b32_e32 v1, v1, v17, vcc
	v_sqrt_f32_e32 v17, v1
	s_nop 0
	v_add_u32_e32 v68, -1, v17
	v_fma_f32 v69, -v68, v17, v1
	v_cmp_ge_f32_e64 s[14:15], 0, v69
	v_add_u32_e32 v69, 1, v17
	s_nop 0
	v_cndmask_b32_e64 v68, v17, v68, s[14:15]
	v_fma_f32 v17, -v69, v17, v1
	v_cmp_lt_f32_e64 s[14:15], 0, v17
	s_nop 1
	v_cndmask_b32_e64 v17, v68, v69, s[14:15]
	v_mul_f32_e32 v68, 0x37800000, v17
	v_cndmask_b32_e32 v17, v17, v68, vcc
	v_cmp_class_f32_e32 vcc, v1, v201
	s_nop 1
	v_cndmask_b32_e32 v1, v17, v1, vcc
	v_div_scale_f32 v17, s[14:15], v1, v1, 1.0
	v_rcp_f32_e32 v68, v17
	s_nop 0
	v_fma_f32 v69, -v17, v68, 1.0
	v_fmac_f32_e32 v68, v69, v68
	v_div_scale_f32 v69, vcc, 1.0, v1, 1.0
	v_mul_f32_e32 v78, v69, v68
	v_fma_f32 v79, -v17, v78, v69
	v_fmac_f32_e32 v78, v79, v68
	v_fma_f32 v17, -v17, v78, v69
	v_div_fmas_f32 v17, v17, v68, v78
	v_div_fixup_f32 v68, v17, v1, 1.0
	v_pk_mul_f32 v[78:79], v[68:69], v[156:157] op_sel_hi:[0,1]
	s_waitcnt lgkmcnt(3)
	v_pk_mul_f32 v[50:51], v[50:51], v[78:79]
	v_mul_f32_e32 v1, 0xbfb8aa3b, v58
	v_pk_mul_f32 v[50:51], v[54:55], v[50:51]
	v_pk_mul_f32 v[54:55], v[68:69], v[150:151] op_sel_hi:[0,1]
	v_pk_mul_f32 v[52:53], v[52:53], v[54:55]
	v_cvt_pk_bf16_f32 v50, v50, v51
	v_pk_mul_f32 v[52:53], v[152:153], v[52:53]
	v_exp_f32_e32 v1, v1
	v_cvt_pk_bf16_f32 v51, v52, v53
	v_pk_mul_f32 v[52:53], v[68:69], v[148:149] op_sel_hi:[0,1]
	s_waitcnt lgkmcnt(2)
	v_pk_mul_f32 v[12:13], v[12:13], v[52:53]
	v_add_f32_e32 v1, 1.0, v1
	v_pk_mul_f32 v[12:13], v[56:57], v[12:13]
	v_ashrrev_i32_e32 v17, 31, v16
	v_cvt_pk_bf16_f32 v52, v12, v13
	v_pk_mul_f32 v[12:13], v[68:69], v[76:77] op_sel_hi:[0,1]
	v_pk_mul_f32 v[12:13], v[14:15], v[12:13]
	s_nop 0
	v_pk_mul_f32 v[12:13], v[80:81], v[12:13]
	s_nop 0
	v_cvt_pk_bf16_f32 v53, v12, v13
	v_pk_mul_f32 v[12:13], v[68:69], v[72:73] op_sel_hi:[0,1]
	s_waitcnt lgkmcnt(1)
	v_pk_mul_f32 v[8:9], v[8:9], v[12:13]
	v_pk_mul_f32 v[12:13], v[68:69], v[66:67] op_sel_hi:[0,1]
	v_pk_mul_f32 v[10:11], v[10:11], v[12:13]
	v_pk_mul_f32 v[8:9], v[74:75], v[8:9]
	v_pk_mul_f32 v[10:11], v[70:71], v[10:11]
	v_cvt_pk_bf16_f32 v8, v8, v9
	v_cvt_pk_bf16_f32 v9, v10, v11
	v_pk_mul_f32 v[10:11], v[68:69], v[62:63] op_sel_hi:[0,1]
	s_waitcnt lgkmcnt(0)
	v_pk_mul_f32 v[4:5], v[4:5], v[10:11]
	v_pk_mul_f32 v[12:13], v[68:69], v[60:61] op_sel_hi:[0,1]
	v_pk_mul_f32 v[4:5], v[64:65], v[4:5]
	v_pk_mul_f32 v[6:7], v[6:7], v[12:13]
	v_cvt_pk_bf16_f32 v10, v4, v5
	v_rcp_f32_e32 v4, v1
	v_mul_f32_e32 v1, 0xbfb8aa3b, v59
	v_exp_f32_e32 v1, v1
	v_mov_b32_e32 v69, v210
	v_mov_b32_e32 v68, v187
	v_add_f32_e32 v1, 1.0, v1
	v_rcp_f32_e32 v5, v1
	s_nop 0
	v_pk_mul_f32 v[4:5], v[4:5], v[58:59]
	s_nop 0
	v_pk_mul_f32 v[4:5], v[4:5], v[6:7]
	s_nop 0
	v_cvt_pk_bf16_f32 v11, v4, v5
	v_lshl_add_u64 v[4:5], s[90:91], 0, v[16:17]
	v_lshlrev_b64 v[4:5], 13, v[4:5]
	v_lshl_add_u64 v[4:5], s[86:87], 0, v[4:5]
	v_lshl_add_u64 v[4:5], v[4:5], 0, v[2:3]
	global_store_dwordx4 v[4:5], v[50:53], off
	global_store_dwordx4 v[4:5], v[8:11], off offset:16
	s_cbranch_scc1 .LBB0_284
